# K-half exchange adds hoisted before the grid-barrier wait; pre-loop block and topic loop regenerated with bank-aware registers on the exchanged-tile layout
# baseline (speedup 1.0000x reference)
.LBB1_53:
	s_or_b64 exec, exec, s[2:3]
	v_or_b32_e32 v198, v212, v214
	v_add_u32_e32 v198, 0x17080, v198
	ds_read_b128 v[36:39], v198
	ds_read_b128 v[40:43], v198 offset:32
	ds_read_b128 v[44:47], v198 offset:64
	ds_read_b128 v[48:51], v198 offset:96
	v_mul_u32_u24_e32 v200, 10, v225
	v_lshlrev_b32_e32 v1, 9, v1
	v_lshlrev_b32_e32 v199, 9, v200
	v_lshl_or_b32 v1, v200, 12, v1
	v_lshlrev_b32_e32 v200, 10, v224
	v_or3_b32 v1, v200, v1, v211
	v_or3_b32 v199, v199, v212, v214
	v_add_u32_e32 v1, 0x2800, v1
	s_waitcnt lgkmcnt(0)
	v_add_f32_e32 v142, v36, v142
	v_add_f32_e32 v143, v37, v143
	v_add_f32_e32 v144, v38, v144
	v_add_f32_e32 v145, v39, v145
	v_add_f32_e32 v138, v40, v138
	v_add_f32_e32 v139, v41, v139
	v_add_f32_e32 v140, v42, v140
	v_add_f32_e32 v141, v43, v141
	v_add_f32_e32 v134, v44, v134
	v_add_f32_e32 v135, v45, v135
	v_add_f32_e32 v136, v46, v136
	v_add_f32_e32 v137, v47, v137
	v_add_f32_e32 v130, v48, v130
	v_add_f32_e32 v131, v49, v131
	v_add_f32_e32 v132, v50, v132
	v_add_f32_e32 v133, v51, v133
	v_add_f32_e32 v126, v36, v126
	v_add_f32_e32 v127, v37, v127
	v_add_f32_e32 v128, v38, v128
	v_add_f32_e32 v129, v39, v129
	v_add_f32_e32 v122, v40, v122
	v_add_f32_e32 v123, v41, v123
	v_add_f32_e32 v124, v42, v124
	v_add_f32_e32 v125, v43, v125
	v_add_f32_e32 v118, v44, v118
	v_add_f32_e32 v119, v45, v119
	v_add_f32_e32 v120, v46, v120
	v_add_f32_e32 v121, v47, v121
	v_add_f32_e32 v114, v48, v114
	v_add_f32_e32 v115, v49, v115
	v_add_f32_e32 v116, v50, v116
	v_add_f32_e32 v117, v51, v117
	v_add_f32_e32 v110, v36, v110
	v_add_f32_e32 v111, v37, v111
	v_add_f32_e32 v112, v38, v112
	v_add_f32_e32 v113, v39, v113
	v_add_f32_e32 v106, v40, v106
	v_add_f32_e32 v107, v41, v107
	v_add_f32_e32 v108, v42, v108
	v_add_f32_e32 v109, v43, v109
	v_add_f32_e32 v98, v44, v98
	v_add_f32_e32 v99, v45, v99
	v_add_f32_e32 v100, v46, v100
	v_add_f32_e32 v101, v47, v101
	v_add_f32_e32 v90, v48, v90
	v_add_f32_e32 v91, v49, v91
	v_add_f32_e32 v92, v50, v92
	v_add_f32_e32 v93, v51, v93
	v_add_f32_e32 v102, v36, v102
	v_add_f32_e32 v103, v37, v103
	v_add_f32_e32 v104, v38, v104
	v_add_f32_e32 v105, v39, v105
	v_add_f32_e32 v94, v40, v94
	v_add_f32_e32 v95, v41, v95
	v_add_f32_e32 v96, v42, v96
	v_add_f32_e32 v97, v43, v97
	v_add_f32_e32 v86, v44, v86
	v_add_f32_e32 v87, v45, v87
	v_add_f32_e32 v88, v46, v88
	v_add_f32_e32 v89, v47, v89
	v_add_f32_e32 v82, v48, v82
	v_add_f32_e32 v83, v49, v83
	v_add_f32_e32 v84, v50, v84
	v_add_f32_e32 v85, v51, v85
	s_waitcnt vmcnt(0)
	v_mul_f32_e32 v66, 0.5, v66
	v_mul_f32_e32 v67, 0.5, v67
	v_mul_f32_e32 v68, 0.5, v68
	v_mul_f32_e32 v69, 0.5, v69
	v_mul_f32_e32 v70, 0.5, v70
	v_mul_f32_e32 v71, 0.5, v71
	v_mul_f32_e32 v72, 0.5, v72
	v_mul_f32_e32 v73, 0.5, v73
	v_mul_f32_e32 v74, 0.5, v74
	v_mul_f32_e32 v75, 0.5, v75
	v_mul_f32_e32 v76, 0.5, v76
	v_mul_f32_e32 v77, 0.5, v77
	v_mul_f32_e32 v78, 0.5, v78
	v_mul_f32_e32 v79, 0.5, v79
	v_mul_f32_e32 v80, 0.5, v80
	v_mul_f32_e32 v81, 0.5, v81
	v_mul_f32_e32 v194, v66, v142
	v_mul_f32_e32 v195, v66, v126
	v_mul_f32_e32 v196, v66, v110
	v_mul_f32_e32 v197, v66, v102
	v_fmac_f32_e32 v194, v67, v143
	v_fmac_f32_e32 v195, v67, v127
	v_fmac_f32_e32 v196, v67, v111
	v_fmac_f32_e32 v197, v67, v103
	v_fmac_f32_e32 v194, v68, v144
	v_fmac_f32_e32 v195, v68, v128
	v_fmac_f32_e32 v196, v68, v112
	v_fmac_f32_e32 v197, v68, v104
	v_fmac_f32_e32 v194, v69, v145
	v_fmac_f32_e32 v195, v69, v129
	v_fmac_f32_e32 v196, v69, v113
	v_fmac_f32_e32 v197, v69, v105
	v_fmac_f32_e32 v194, v70, v138
	v_fmac_f32_e32 v195, v70, v122
	v_fmac_f32_e32 v196, v70, v106
	v_fmac_f32_e32 v197, v70, v94
	v_fmac_f32_e32 v194, v71, v139
	v_fmac_f32_e32 v195, v71, v123
	v_fmac_f32_e32 v196, v71, v107
	v_fmac_f32_e32 v197, v71, v95
	v_fmac_f32_e32 v194, v72, v140
	v_fmac_f32_e32 v195, v72, v124
	v_fmac_f32_e32 v196, v72, v108
	v_fmac_f32_e32 v197, v72, v96
	v_fmac_f32_e32 v194, v73, v141
	v_fmac_f32_e32 v195, v73, v125
	v_fmac_f32_e32 v196, v73, v109
	v_fmac_f32_e32 v197, v73, v97
	v_fmac_f32_e32 v194, v74, v134
	v_fmac_f32_e32 v195, v74, v118
	v_fmac_f32_e32 v196, v74, v98
	v_fmac_f32_e32 v197, v74, v86
	v_fmac_f32_e32 v194, v75, v135
	v_fmac_f32_e32 v195, v75, v119
	v_fmac_f32_e32 v196, v75, v99
	v_fmac_f32_e32 v197, v75, v87
	v_fmac_f32_e32 v194, v76, v136
	v_fmac_f32_e32 v195, v76, v120
	v_fmac_f32_e32 v196, v76, v100
	v_fmac_f32_e32 v197, v76, v88
	v_fmac_f32_e32 v194, v77, v137
	v_fmac_f32_e32 v195, v77, v121
	v_fmac_f32_e32 v196, v77, v101
	v_fmac_f32_e32 v197, v77, v89
	v_fmac_f32_e32 v194, v78, v130
	v_fmac_f32_e32 v195, v78, v114
	v_fmac_f32_e32 v196, v78, v90
	v_fmac_f32_e32 v197, v78, v82
	v_fmac_f32_e32 v194, v79, v131
	v_fmac_f32_e32 v195, v79, v115
	v_fmac_f32_e32 v196, v79, v91
	v_fmac_f32_e32 v197, v79, v83
	v_fmac_f32_e32 v194, v80, v132
	v_fmac_f32_e32 v195, v80, v116
	v_fmac_f32_e32 v196, v80, v92
	v_fmac_f32_e32 v197, v80, v84
	v_fmac_f32_e32 v194, v81, v133
	v_fmac_f32_e32 v195, v81, v117
	v_fmac_f32_e32 v196, v81, v93
	v_fmac_f32_e32 v197, v81, v85
	s_mov_b32 s0, 0
	v_add_u32_e32 v198, s0, v199
	ds_read_b128 v[4:7], v198
	ds_read_b128 v[8:11], v198 offset:32
	ds_read_b128 v[12:15], v198 offset:64
	ds_read_b128 v[16:19], v198 offset:96
	s_addk_i32 s0, 0x200
.Ltopic_loop:
	v_add_u32_e32 v198, s0, v199
	ds_read_b128 v[20:23], v198
	ds_read_b128 v[24:27], v198 offset:32
	ds_read_b128 v[28:31], v198 offset:64
	ds_read_b128 v[32:35], v198 offset:96
	s_addk_i32 s0, 0x200
	s_waitcnt lgkmcnt(4)
	v_add_f32_e32 v36, v142, v4
	v_add_f32_e32 v40, v126, v4
	v_add_f32_e32 v44, v110, v4
	v_add_f32_e32 v48, v102, v4
	v_add_f32_e32 v37, v143, v5
	v_add_f32_e32 v41, v127, v5
	v_add_f32_e32 v45, v111, v5
	v_add_f32_e32 v49, v103, v5
	v_add_f32_e32 v38, v144, v6
	v_add_f32_e32 v42, v128, v6
	v_add_f32_e32 v46, v112, v6
	v_add_f32_e32 v50, v104, v6
	v_add_f32_e32 v39, v145, v7
	v_add_f32_e32 v43, v129, v7
	v_add_f32_e32 v47, v113, v7
	v_add_f32_e32 v51, v105, v7
	v_mul_f32_e32 v193, v66, v4
	v_fma_f32 v185, v66, |v36|, v194
	v_fma_f32 v187, v66, |v40|, v195
	v_fma_f32 v189, v66, |v44|, v196
	v_fma_f32 v191, v66, |v48|, v197
	v_mul_f32_e32 v192, v67, v5
	v_mul_f32_e64 v184, v67, |v37|
	v_mul_f32_e64 v186, v67, |v41|
	v_mul_f32_e64 v188, v67, |v45|
	v_mul_f32_e64 v190, v67, |v49|
	v_fmac_f32_e32 v193, v68, v6
	v_fma_f32 v185, v68, |v38|, v185
	v_fma_f32 v187, v68, |v42|, v187
	v_fma_f32 v189, v68, |v46|, v189
	v_fma_f32 v191, v68, |v50|, v191
	v_fmac_f32_e32 v192, v69, v7
	v_fma_f32 v184, v69, |v39|, v184
	v_fma_f32 v186, v69, |v43|, v186
	v_fma_f32 v188, v69, |v47|, v188
	v_fma_f32 v190, v69, |v51|, v190
	v_add_f32_e32 v168, v138, v8
	v_add_f32_e32 v172, v122, v8
	v_add_f32_e32 v176, v106, v8
	v_add_f32_e32 v180, v94, v8
	v_add_f32_e32 v169, v139, v9
	v_add_f32_e32 v173, v123, v9
	v_add_f32_e32 v177, v107, v9
	v_add_f32_e32 v181, v95, v9
	v_add_f32_e32 v170, v140, v10
	v_add_f32_e32 v174, v124, v10
	v_add_f32_e32 v178, v108, v10
	v_add_f32_e32 v182, v96, v10
	v_add_f32_e32 v171, v141, v11
	v_add_f32_e32 v175, v125, v11
	v_add_f32_e32 v179, v109, v11
	v_add_f32_e32 v183, v97, v11
	v_fmac_f32_e32 v193, v70, v8
	v_fma_f32 v185, v70, |v168|, v185
	v_fma_f32 v187, v70, |v172|, v187
	v_fma_f32 v189, v70, |v176|, v189
	v_fma_f32 v191, v70, |v180|, v191
	v_fmac_f32_e32 v192, v71, v9
	v_fma_f32 v184, v71, |v169|, v184
	v_fma_f32 v186, v71, |v173|, v186
	v_fma_f32 v188, v71, |v177|, v188
	v_fma_f32 v190, v71, |v181|, v190
	v_fmac_f32_e32 v193, v72, v10
	v_fma_f32 v185, v72, |v170|, v185
	v_fma_f32 v187, v72, |v174|, v187
	v_fma_f32 v189, v72, |v178|, v189
	v_fma_f32 v191, v72, |v182|, v191
	v_fmac_f32_e32 v192, v73, v11
	v_fma_f32 v184, v73, |v171|, v184
	v_fma_f32 v186, v73, |v175|, v186
	v_fma_f32 v188, v73, |v179|, v188
	v_fma_f32 v190, v73, |v183|, v190
	v_add_f32_e32 v36, v134, v12
	v_add_f32_e32 v40, v118, v12
	v_add_f32_e32 v44, v98, v12
	v_add_f32_e32 v48, v86, v12
	v_add_f32_e32 v37, v135, v13
	v_add_f32_e32 v41, v119, v13
	v_add_f32_e32 v45, v99, v13
	v_add_f32_e32 v49, v87, v13
	v_add_f32_e32 v38, v136, v14
	v_add_f32_e32 v42, v120, v14
	v_add_f32_e32 v46, v100, v14
	v_add_f32_e32 v50, v88, v14
	v_add_f32_e32 v39, v137, v15
	v_add_f32_e32 v43, v121, v15
	v_add_f32_e32 v47, v101, v15
	v_add_f32_e32 v51, v89, v15
	v_fmac_f32_e32 v193, v74, v12
	v_fma_f32 v185, v74, |v36|, v185
	v_fma_f32 v187, v74, |v40|, v187
	v_fma_f32 v189, v74, |v44|, v189
	v_fma_f32 v191, v74, |v48|, v191
	v_fmac_f32_e32 v192, v75, v13
	v_fma_f32 v184, v75, |v37|, v184
	v_fma_f32 v186, v75, |v41|, v186
	v_fma_f32 v188, v75, |v45|, v188
	v_fma_f32 v190, v75, |v49|, v190
	v_fmac_f32_e32 v193, v76, v14
	v_fma_f32 v185, v76, |v38|, v185
	v_fma_f32 v187, v76, |v42|, v187
	v_fma_f32 v189, v76, |v46|, v189
	v_fma_f32 v191, v76, |v50|, v191
	v_fmac_f32_e32 v192, v77, v15
	v_fma_f32 v184, v77, |v39|, v184
	v_fma_f32 v186, v77, |v43|, v186
	v_fma_f32 v188, v77, |v47|, v188
	v_fma_f32 v190, v77, |v51|, v190
	v_add_f32_e32 v168, v130, v16
	v_add_f32_e32 v172, v114, v16
	v_add_f32_e32 v176, v90, v16
	v_add_f32_e32 v180, v82, v16
	v_add_f32_e32 v169, v131, v17
	v_add_f32_e32 v173, v115, v17
	v_add_f32_e32 v177, v91, v17
	v_add_f32_e32 v181, v83, v17
	v_add_f32_e32 v170, v132, v18
	v_add_f32_e32 v174, v116, v18
	v_add_f32_e32 v178, v92, v18
	v_add_f32_e32 v182, v84, v18
	v_add_f32_e32 v171, v133, v19
	v_add_f32_e32 v175, v117, v19
	v_add_f32_e32 v179, v93, v19
	v_add_f32_e32 v183, v85, v19
	v_fmac_f32_e32 v193, v78, v16
	v_fma_f32 v185, v78, |v168|, v185
	v_fma_f32 v187, v78, |v172|, v187
	v_fma_f32 v189, v78, |v176|, v189
	v_fma_f32 v191, v78, |v180|, v191
	v_fmac_f32_e32 v192, v79, v17
	v_fma_f32 v184, v79, |v169|, v184
	v_fma_f32 v186, v79, |v173|, v186
	v_fma_f32 v188, v79, |v177|, v188
	v_fma_f32 v190, v79, |v181|, v190
	v_fmac_f32_e32 v193, v80, v18
	v_fma_f32 v185, v80, |v170|, v185
	v_fma_f32 v187, v80, |v174|, v187
	v_fma_f32 v189, v80, |v178|, v189
	v_fma_f32 v191, v80, |v182|, v191
	v_fmac_f32_e32 v192, v81, v19
	v_fma_f32 v184, v81, |v171|, v184
	v_fma_f32 v186, v81, |v175|, v186
	v_fma_f32 v188, v81, |v179|, v188
	v_fma_f32 v190, v81, |v183|, v190
	v_add_f32_e32 v193, v193, v192
	v_add_f32_e32 v185, v185, v184
	v_add_f32_e32 v187, v187, v186
	v_add_f32_e32 v189, v189, v188
	v_add_f32_e32 v191, v191, v190
	v_add_f32_e32 v185, v185, v193
	v_add_f32_e32 v187, v187, v193
	v_add_f32_e32 v189, v189, v193
	v_add_f32_e32 v191, v191, v193
	ds_write2_b32 v1, v185, v187 offset1:32
	ds_write2_b32 v1, v189, v191 offset0:64 offset1:96
	v_add_u32_e32 v1, 0x1000, v1
	v_add_u32_e32 v198, s0, v199
	ds_read_b128 v[4:7], v198
	ds_read_b128 v[8:11], v198 offset:32
	ds_read_b128 v[12:15], v198 offset:64
	ds_read_b128 v[16:19], v198 offset:96
	s_addk_i32 s0, 0x200
	s_waitcnt lgkmcnt(4)
	v_add_f32_e32 v36, v142, v20
	v_add_f32_e32 v40, v126, v20
	v_add_f32_e32 v44, v110, v20
	v_add_f32_e32 v48, v102, v20
	v_add_f32_e32 v37, v143, v21
	v_add_f32_e32 v41, v127, v21
	v_add_f32_e32 v45, v111, v21
	v_add_f32_e32 v49, v103, v21
	v_add_f32_e32 v38, v144, v22
	v_add_f32_e32 v42, v128, v22
	v_add_f32_e32 v46, v112, v22
	v_add_f32_e32 v50, v104, v22
	v_add_f32_e32 v39, v145, v23
	v_add_f32_e32 v43, v129, v23
	v_add_f32_e32 v47, v113, v23
	v_add_f32_e32 v51, v105, v23
	v_mul_f32_e32 v193, v66, v20
	v_fma_f32 v185, v66, |v36|, v194
	v_fma_f32 v187, v66, |v40|, v195
	v_fma_f32 v189, v66, |v44|, v196
	v_fma_f32 v191, v66, |v48|, v197
	v_mul_f32_e32 v192, v67, v21
	v_mul_f32_e64 v184, v67, |v37|
	v_mul_f32_e64 v186, v67, |v41|
	v_mul_f32_e64 v188, v67, |v45|
	v_mul_f32_e64 v190, v67, |v49|
	v_fmac_f32_e32 v193, v68, v22
	v_fma_f32 v185, v68, |v38|, v185
	v_fma_f32 v187, v68, |v42|, v187
	v_fma_f32 v189, v68, |v46|, v189
	v_fma_f32 v191, v68, |v50|, v191
	v_fmac_f32_e32 v192, v69, v23
	v_fma_f32 v184, v69, |v39|, v184
	v_fma_f32 v186, v69, |v43|, v186
	v_fma_f32 v188, v69, |v47|, v188
	v_fma_f32 v190, v69, |v51|, v190
	v_add_f32_e32 v168, v138, v24
	v_add_f32_e32 v172, v122, v24
	v_add_f32_e32 v176, v106, v24
	v_add_f32_e32 v180, v94, v24
	v_add_f32_e32 v169, v139, v25
	v_add_f32_e32 v173, v123, v25
	v_add_f32_e32 v177, v107, v25
	v_add_f32_e32 v181, v95, v25
	v_add_f32_e32 v170, v140, v26
	v_add_f32_e32 v174, v124, v26
	v_add_f32_e32 v178, v108, v26
	v_add_f32_e32 v182, v96, v26
	v_add_f32_e32 v171, v141, v27
	v_add_f32_e32 v175, v125, v27
	v_add_f32_e32 v179, v109, v27
	v_add_f32_e32 v183, v97, v27
	v_fmac_f32_e32 v193, v70, v24
	v_fma_f32 v185, v70, |v168|, v185
	v_fma_f32 v187, v70, |v172|, v187
	v_fma_f32 v189, v70, |v176|, v189
	v_fma_f32 v191, v70, |v180|, v191
	v_fmac_f32_e32 v192, v71, v25
	v_fma_f32 v184, v71, |v169|, v184
	v_fma_f32 v186, v71, |v173|, v186
	v_fma_f32 v188, v71, |v177|, v188
	v_fma_f32 v190, v71, |v181|, v190
	v_fmac_f32_e32 v193, v72, v26
	v_fma_f32 v185, v72, |v170|, v185
	v_fma_f32 v187, v72, |v174|, v187
	v_fma_f32 v189, v72, |v178|, v189
	v_fma_f32 v191, v72, |v182|, v191
	v_fmac_f32_e32 v192, v73, v27
	v_fma_f32 v184, v73, |v171|, v184
	v_fma_f32 v186, v73, |v175|, v186
	v_fma_f32 v188, v73, |v179|, v188
	v_fma_f32 v190, v73, |v183|, v190
	v_add_f32_e32 v36, v134, v28
	v_add_f32_e32 v40, v118, v28
	v_add_f32_e32 v44, v98, v28
	v_add_f32_e32 v48, v86, v28
	v_add_f32_e32 v37, v135, v29
	v_add_f32_e32 v41, v119, v29
	v_add_f32_e32 v45, v99, v29
	v_add_f32_e32 v49, v87, v29
	v_add_f32_e32 v38, v136, v30
	v_add_f32_e32 v42, v120, v30
	v_add_f32_e32 v46, v100, v30
	v_add_f32_e32 v50, v88, v30
	v_add_f32_e32 v39, v137, v31
	v_add_f32_e32 v43, v121, v31
	v_add_f32_e32 v47, v101, v31
	v_add_f32_e32 v51, v89, v31
	v_fmac_f32_e32 v193, v74, v28
	v_fma_f32 v185, v74, |v36|, v185
	v_fma_f32 v187, v74, |v40|, v187
	v_fma_f32 v189, v74, |v44|, v189
	v_fma_f32 v191, v74, |v48|, v191
	v_fmac_f32_e32 v192, v75, v29
	v_fma_f32 v184, v75, |v37|, v184
	v_fma_f32 v186, v75, |v41|, v186
	v_fma_f32 v188, v75, |v45|, v188
	v_fma_f32 v190, v75, |v49|, v190
	v_fmac_f32_e32 v193, v76, v30
	v_fma_f32 v185, v76, |v38|, v185
	v_fma_f32 v187, v76, |v42|, v187
	v_fma_f32 v189, v76, |v46|, v189
	v_fma_f32 v191, v76, |v50|, v191
	v_fmac_f32_e32 v192, v77, v31
	v_fma_f32 v184, v77, |v39|, v184
	v_fma_f32 v186, v77, |v43|, v186
	v_fma_f32 v188, v77, |v47|, v188
	v_fma_f32 v190, v77, |v51|, v190
	v_add_f32_e32 v168, v130, v32
	v_add_f32_e32 v172, v114, v32
	v_add_f32_e32 v176, v90, v32
	v_add_f32_e32 v180, v82, v32
	v_add_f32_e32 v169, v131, v33
	v_add_f32_e32 v173, v115, v33
	v_add_f32_e32 v177, v91, v33
	v_add_f32_e32 v181, v83, v33
	v_add_f32_e32 v170, v132, v34
	v_add_f32_e32 v174, v116, v34
	v_add_f32_e32 v178, v92, v34
	v_add_f32_e32 v182, v84, v34
	v_add_f32_e32 v171, v133, v35
	v_add_f32_e32 v175, v117, v35
	v_add_f32_e32 v179, v93, v35
	v_add_f32_e32 v183, v85, v35
	v_fmac_f32_e32 v193, v78, v32
	v_fma_f32 v185, v78, |v168|, v185
	v_fma_f32 v187, v78, |v172|, v187
	v_fma_f32 v189, v78, |v176|, v189
	v_fma_f32 v191, v78, |v180|, v191
	v_fmac_f32_e32 v192, v79, v33
	v_fma_f32 v184, v79, |v169|, v184
	v_fma_f32 v186, v79, |v173|, v186
	v_fma_f32 v188, v79, |v177|, v188
	v_fma_f32 v190, v79, |v181|, v190
	v_fmac_f32_e32 v193, v80, v34
	v_fma_f32 v185, v80, |v170|, v185
	v_fma_f32 v187, v80, |v174|, v187
	v_fma_f32 v189, v80, |v178|, v189
	v_fma_f32 v191, v80, |v182|, v191
	v_fmac_f32_e32 v192, v81, v35
	v_fma_f32 v184, v81, |v171|, v184
	v_fma_f32 v186, v81, |v175|, v186
	v_fma_f32 v188, v81, |v179|, v188
	v_fma_f32 v190, v81, |v183|, v190
	v_add_f32_e32 v193, v193, v192
	v_add_f32_e32 v185, v185, v184
	v_add_f32_e32 v187, v187, v186
	v_add_f32_e32 v189, v189, v188
	v_add_f32_e32 v191, v191, v190
	v_add_f32_e32 v185, v185, v193
	v_add_f32_e32 v187, v187, v193
	v_add_f32_e32 v189, v189, v193
	v_add_f32_e32 v191, v191, v193
	ds_write2_b32 v1, v185, v187 offset1:32
	ds_write2_b32 v1, v189, v191 offset0:64 offset1:96
	v_add_u32_e32 v1, 0x1000, v1
	s_cmpk_eq_i32 s0, 0x1600
	s_cbranch_scc0 .Ltopic_loop
	v_lshl_or_b32 v1, v227, 12, v226
	s_waitcnt lgkmcnt(0)
	s_barrier
	ds_read2st64_b32 v[2:3], v1 offset0:40 offset1:42
	ds_read2st64_b32 v[4:5], v1 offset0:44 offset1:46
	ds_read2st64_b32 v[6:7], v1 offset0:48 offset1:50
	v_or_b32_e32 v13, 16, v227
	s_waitcnt lgkmcnt(2)
	v_add_f32_e32 v2, s18, v2
	v_add_f32_e32 v8, v2, v3
	ds_read2st64_b32 v[2:3], v1 offset0:52 offset1:54
	s_waitcnt lgkmcnt(2)
	v_add_f32_e32 v4, v8, v4
	v_add_f32_e32 v4, v4, v5
	s_waitcnt lgkmcnt(1)
	v_add_f32_e32 v4, v4, v6
	v_add_f32_e32 v4, v4, v7
	s_waitcnt lgkmcnt(0)
	v_add_f32_e32 v2, v4, v2
	v_add_f32_e32 v2, v2, v3
	v_mul_f32_e32 v2, 0xbfb8aa3b, v2
	v_exp_f32_e32 v2, v2
	s_nop 0
	v_add_f32_e32 v4, 1.0, v2
	v_div_scale_f32 v5, s[0:1], v4, v4, 1.0
	v_rcp_f32_e32 v6, v5
	v_div_scale_f32 v7, vcc, 1.0, v4, 1.0
	ds_read2st64_b32 v[2:3], v1 offset0:104 offset1:106
	v_fma_f32 v8, -v5, v6, 1.0
	v_fmac_f32_e32 v6, v8, v6
	v_mul_f32_e32 v8, v7, v6
	v_fma_f32 v9, -v5, v8, v7
	v_fmac_f32_e32 v8, v9, v6
	v_fma_f32 v5, -v5, v8, v7
	v_div_fmas_f32 v5, v5, v6, v8
	v_div_fixup_f32 v8, v5, v4, 1.0
	ds_read2st64_b32 v[4:5], v1 offset0:108 offset1:110
	ds_read2st64_b32 v[6:7], v1 offset0:112 offset1:114
	s_waitcnt lgkmcnt(2)
	v_add_f32_e32 v2, s18, v2
	v_add_f32_e32 v9, v2, v3
	ds_read2st64_b32 v[2:3], v1 offset0:116 offset1:118
	s_waitcnt lgkmcnt(2)
	v_add_f32_e32 v4, v9, v4
	v_add_f32_e32 v4, v4, v5
	s_waitcnt lgkmcnt(1)
	v_add_f32_e32 v4, v4, v6
	v_add_f32_e32 v4, v4, v7
	s_waitcnt lgkmcnt(0)
	v_add_f32_e32 v2, v4, v2
	v_add_f32_e32 v2, v2, v3
	v_mul_f32_e32 v2, 0xbfb8aa3b, v2
	v_exp_f32_e32 v2, v2
	v_lshlrev_b32_e32 v3, 2, v227
	v_or_b32_e32 v6, 8, v227
	v_mov_b32_e32 v7, 0x17000
	v_add_f32_e32 v10, 1.0, v2
	v_div_scale_f32 v5, s[0:1], v10, v10, 1.0
	v_rcp_f32_e32 v11, v5
	v_or_b32_e32 v4, 0x17000, v3
	v_lshl_or_b32 v12, v6, 2, v7
	v_or_b32_e32 v2, 0x17010, v3
	v_or_b32_e32 v3, 0x17030, v3
	v_lshl_or_b32 v7, v13, 2, v7
	ds_read_b32 v4, v4
	ds_read_b32 v14, v2
	ds_read_b32 v12, v12
	ds_read_b32 v15, v3
	ds_read_b32 v16, v7
	s_waitcnt lgkmcnt(4)
	v_fmaak_f32 v2, v8, v4, 0xbc23d70a
	v_max_f32_e32 v8, 0, v2
	v_fma_f32 v2, -v5, v11, 1.0
	v_fmac_f32_e32 v11, v2, v11
	v_div_scale_f32 v4, vcc, 1.0, v10, 1.0
	v_mul_f32_e32 v17, v4, v11
	v_lshl_or_b32 v18, v6, 12, v226
	ds_read2st64_b32 v[2:3], v18 offset0:40 offset1:42
	v_fma_f32 v6, -v5, v17, v4
	v_fmac_f32_e32 v17, v6, v11
	v_fma_f32 v19, -v5, v17, v4
	ds_read2st64_b32 v[4:5], v18 offset0:44 offset1:46
	ds_read2st64_b32 v[6:7], v18 offset0:48 offset1:50
	s_waitcnt lgkmcnt(2)
	v_add_f32_e32 v2, s18, v2
	v_add_f32_e32 v20, v2, v3
	ds_read2st64_b32 v[2:3], v18 offset0:52 offset1:54
	s_waitcnt lgkmcnt(2)
	v_add_f32_e32 v4, v20, v4
	v_add_f32_e32 v4, v4, v5
	s_waitcnt lgkmcnt(1)
	v_add_f32_e32 v4, v4, v6
	v_add_f32_e32 v4, v4, v7
	s_waitcnt lgkmcnt(0)
	v_add_f32_e32 v2, v4, v2
	v_add_f32_e32 v2, v2, v3
	v_mul_f32_e32 v2, 0xbfb8aa3b, v2
	v_exp_f32_e32 v2, v2
	v_div_fmas_f32 v3, v19, v11, v17
	v_div_fixup_f32 v3, v3, v10, 1.0
	v_mov_b32_e32 v9, 0xbc23d70a
	v_add_f32_e32 v10, 1.0, v2
	v_div_scale_f32 v4, s[0:1], v10, v10, 1.0
	v_rcp_f32_e32 v11, v4
	v_fmaak_f32 v2, v3, v14, 0xbc23d70a
	v_max_f32_e32 v2, 0, v2
	v_add_f32_e32 v8, v8, v2
	v_fma_f32 v2, -v4, v11, 1.0
	v_fmac_f32_e32 v11, v2, v11
	v_div_scale_f32 v5, vcc, 1.0, v10, 1.0
	v_mul_f32_e32 v14, v5, v11
	ds_read2st64_b32 v[2:3], v1 offset0:232 offset1:234
	v_fma_f32 v6, -v4, v14, v5
	v_fmac_f32_e32 v14, v6, v11
	v_fma_f32 v17, -v4, v14, v5
	ds_read2st64_b32 v[4:5], v1 offset0:236 offset1:238
	ds_read2st64_b32 v[6:7], v1 offset0:240 offset1:242
	s_waitcnt lgkmcnt(2)
	v_add_f32_e32 v2, s18, v2
	v_add_f32_e32 v18, v2, v3
	ds_read2st64_b32 v[2:3], v1 offset0:244 offset1:246
	s_waitcnt lgkmcnt(2)
	v_add_f32_e32 v1, v18, v4
	v_add_f32_e32 v1, v1, v5
	s_waitcnt lgkmcnt(1)
	v_add_f32_e32 v1, v1, v6
	v_add_f32_e32 v1, v1, v7
	s_waitcnt lgkmcnt(0)
	v_add_f32_e32 v1, v1, v2
	v_add_f32_e32 v1, v1, v3
	v_mul_f32_e32 v1, 0xbfb8aa3b, v1
	v_exp_f32_e32 v1, v1
	v_div_fmas_f32 v2, v17, v11, v14
	v_div_fixup_f32 v2, v2, v10, 1.0
	v_fmaak_f32 v2, v2, v12, 0xbc23d70a
	v_add_f32_e32 v1, 1.0, v1
	v_div_scale_f32 v4, s[0:1], v1, v1, 1.0
	v_rcp_f32_e32 v10, v4
	v_max_f32_e32 v2, 0, v2
	v_add_f32_e32 v8, v8, v2
	v_div_scale_f32 v5, vcc, 1.0, v1, 1.0
	v_fma_f32 v2, -v4, v10, 1.0
	v_fmac_f32_e32 v10, v2, v10
	v_mul_f32_e32 v11, v5, v10
	v_lshl_or_b32 v12, v13, 12, v226
	ds_read2st64_b32 v[2:3], v12 offset0:40 offset1:42
	v_fma_f32 v6, -v4, v11, v5
	v_fmac_f32_e32 v11, v6, v10
	v_fma_f32 v13, -v4, v11, v5
	ds_read2st64_b32 v[4:5], v12 offset0:44 offset1:46
	ds_read2st64_b32 v[6:7], v12 offset0:48 offset1:50
	s_waitcnt lgkmcnt(2)
	v_add_f32_e32 v2, s18, v2
	v_add_f32_e32 v14, v2, v3
	ds_read2st64_b32 v[2:3], v12 offset0:52 offset1:54
	s_waitcnt lgkmcnt(2)
	v_add_f32_e32 v4, v14, v4
	v_add_f32_e32 v4, v4, v5
	s_waitcnt lgkmcnt(1)
	v_add_f32_e32 v4, v4, v6
	v_add_f32_e32 v4, v4, v7
	s_waitcnt lgkmcnt(0)
	v_add_f32_e32 v2, v4, v2
	v_add_f32_e32 v2, v2, v3
	v_mul_f32_e32 v2, 0xbfb8aa3b, v2
	v_exp_f32_e32 v2, v2
	v_div_fmas_f32 v3, v13, v10, v11
	v_div_fixup_f32 v1, v3, v1, 1.0
	v_fmaak_f32 v1, v1, v15, 0xbc23d70a
	v_add_f32_e32 v2, 1.0, v2
	v_div_scale_f32 v3, s[0:1], v2, v2, 1.0
	v_rcp_f32_e32 v4, v3
	v_max_f32_e32 v1, 0, v1
	v_add_f32_e32 v1, v8, v1
	s_lshl_b32 s0, s42, 5
	v_fma_f32 v5, -v3, v4, 1.0
	v_fmac_f32_e32 v4, v5, v4
	v_div_scale_f32 v5, vcc, 1.0, v2, 1.0
	v_mul_f32_e32 v6, v5, v4
	v_fma_f32 v7, -v3, v6, v5
	v_fmac_f32_e32 v6, v7, v4
	v_fma_f32 v3, -v3, v6, v5
	v_div_fmas_f32 v3, v3, v4, v6
	v_div_fixup_f32 v2, v3, v2, 1.0
	v_fmac_f32_e32 v9, v2, v16
	v_max_f32_e32 v2, 0, v9
	v_add_f32_e32 v2, v1, v2
	v_mov_b32_e32 v1, 0x16800
	v_lshl_or_b32 v1, v0, 2, v1
	v_cmp_gt_u32_e32 vcc, s0, v0
	ds_write_b32 v1, v2
	s_waitcnt lgkmcnt(0)
	s_barrier
	s_and_saveexec_b64 s[0:1], vcc
	s_cbranch_execz .LBB1_57
	ds_read2st64_b32 v[2:3], v1 offset1:2
	ds_read2st64_b32 v[4:5], v1 offset0:4 offset1:6
	v_add_u32_e32 v0, s33, v0
	v_ashrrev_i32_e32 v1, 31, v0
	v_lshl_add_u64 v[6:7], v[0:1], 2, s[10:11]
	s_waitcnt lgkmcnt(1)
	v_add_f32_e32 v1, v2, v3
	s_waitcnt lgkmcnt(0)
	v_add_f32_e32 v1, v1, v4
	v_add_f32_e32 v1, v1, v5
	v_add_u32_e32 v0, 0x7d00, v0
	v_mul_f32_e32 v2, 0x3d4ccccd, v1
	v_ashrrev_i32_e32 v1, 31, v0
	v_lshl_add_u64 v[0:1], v[0:1], 2, s[10:11]
	global_store_dword v[6:7], v2, off
	global_store_dword v[0:1], v2, off
